# speedup vs baseline: 1.0009x; 1.0009x over previous
.LBB0_89:
	s_or_b64 exec, exec, s[8:9]
	v_mov_b32_e32 v3, 0
	v_lshlrev_b32_e32 v70, 4, v28
	s_and_saveexec_b64 s[60:61], vcc
	s_cbranch_execz .LBB0_118
	v_mov_b32_e32 v87, 0x10000
	v_lshl_add_u64 v[22:23], s[12:13], 0, v[2:3]
	s_waitcnt vmcnt(0)
	v_cndmask_b32_e64 v55, v87, v4, s[0:1]
	s_movk_i32 s0, 0x880
	v_mov_b32_e32 v2, 0x1dd00
	v_mad_u32_u24 v4, v80, s0, v2
	v_lshlrev_b32_e32 v2, 1, v1
	v_mov_b32_e32 v27, v3
	v_lshl_add_u64 v[74:75], s[14:15], 0, v[2:3]
	v_mbcnt_hi_u32_b32 v2, -1, v29
	v_lshl_add_u64 v[72:73], v[22:23], 0, v[26:27]
	v_and_b32_e32 v23, 64, v2
	v_xor_b32_e32 v22, 16, v2
	v_add_u32_e32 v23, 64, v23
	v_cmp_lt_i32_e32 vcc, v22, v23
	v_lshlrev_b32_e32 v88, 2, v28
	v_and_b32_e32 v24, 7, v0
	v_cndmask_b32_e32 v22, v2, v22, vcc
	v_lshlrev_b32_e32 v90, 2, v22
	v_xor_b32_e32 v22, 32, v2
	v_cmp_lt_i32_e32 vcc, v22, v23
	s_mov_b32 s24, 0x10000
	v_mov_b32_e32 v71, v3
	v_cndmask_b32_e32 v2, v2, v22, vcc
	v_lshlrev_b32_e32 v91, 2, v2
	v_lshrrev_b32_e32 v2, 2, v79
	v_mul_u32_u24_e32 v22, 0x88, v79
	v_add3_u32 v92, v4, v22, v1
	v_or_b32_e32 v2, v88, v2
	v_lshlrev_b32_e32 v22, 3, v0
	v_mul_u32_u24_e32 v2, 0x88, v2
	v_and_b32_e32 v22, 24, v22
	v_add3_u32 v93, v4, v2, v22
	v_lshlrev_b32_e32 v2, 6, v24
	v_lshl_add_u64 v[22:23], s[22:23], 0, v[2:3]
	v_lshlrev_b32_e32 v2, 5, v24
	v_or3_b32 v78, v2, v1, s24
	v_bfe_u32 v2, v0, 1, 2
	v_lshrrev_b32_e32 v89, 3, v79
	v_cmp_eq_u32_e64 s[6:7], 4, v24
	v_cmp_eq_u32_e64 s[8:9], 3, v24
	v_cmp_eq_u32_e64 s[10:11], 2, v24
	v_cmp_eq_u32_e64 s[12:13], 1, v24
	v_cmp_eq_u32_e64 s[14:15], 0, v24
	v_cmp_eq_u32_e64 s[16:17], 7, v24
	v_cmp_eq_u32_e64 s[18:19], 6, v24
	v_cmp_eq_u32_e64 s[20:21], 5, v24
	v_lshl_add_u64 v[76:77], v[22:23], 0, v[70:71]
	v_cmp_eq_u32_e64 s[22:23], 0, v2
	v_cmp_eq_u32_e64 s[24:25], 1, v2
	v_cmp_eq_u32_e64 s[26:27], 2, v2
	v_cmp_eq_u32_e64 s[28:29], 3, v2
	s_and_b64 s[22:23], s[22:23], s[4:5]
	s_and_b64 s[24:25], s[24:25], s[4:5]
	s_and_b64 s[26:27], s[26:27], s[4:5]
	s_and_b64 s[28:29], s[28:29], s[4:5]
	v_mov_b32_e32 v71, 0xf149f2ca
	s_mov_b64 s[62:63], 0
	s_mov_b32 s69, 0xf149f2ca
	s_mov_b32 s70, 0xefa18f08
	s_mov_b32 s71, 0x41000000
	s_movk_i32 s72, 0x110
	v_mov_b32_e32 v94, 0x26b40
	v_mov_b32_e32 v95, 0x26500
	v_mov_b32_e32 v96, 0x2650c
	v_mov_b32_e32 v100, 0
	v_mov_b32_e32 v4, 0
	v_mov_b32_e32 v103, 0xf149f2ca
	v_mov_b32_e32 v46, v3
	v_mov_b32_e32 v47, v3
	v_mov_b32_e32 v48, v3
	v_mov_b32_e32 v49, v3
	v_mov_b32_e32 v50, v3
	v_mov_b32_e32 v51, v3
	v_mov_b32_e32 v52, v3
	v_mov_b32_e32 v53, v3
	v_mov_b32_e32 v38, v3
	v_mov_b32_e32 v39, v3
	v_mov_b32_e32 v40, v3
	v_mov_b32_e32 v41, v3
	v_mov_b32_e32 v42, v3
	v_mov_b32_e32 v43, v3
	v_mov_b32_e32 v44, v3
	v_mov_b32_e32 v45, v3
	v_mov_b32_e32 v30, v3
	v_mov_b32_e32 v31, v3
	v_mov_b32_e32 v32, v3
	v_mov_b32_e32 v33, v3
	v_mov_b32_e32 v34, v3
	v_mov_b32_e32 v35, v3
	v_mov_b32_e32 v36, v3
	v_mov_b32_e32 v37, v3
	v_mov_b32_e32 v22, v3
	v_mov_b32_e32 v23, v3
	v_mov_b32_e32 v24, v3
	v_mov_b32_e32 v25, v3
	v_mov_b32_e32 v26, v3
	v_mov_b32_e32 v28, v3
	v_mov_b32_e32 v29, v3
	s_branch .LBB0_95

.LBB0_95:
	v_mov_b32_e32 v97, v54
	v_lshl_or_b32 v2, v84, 4, v79
	v_cmp_gt_i32_e64 s[34:35], s68, v97
	v_lshlrev_b32_e32 v108, 4, v100
	v_add_u32_e32 v100, 16, v108
	v_cmp_ge_i32_e64 s[0:1], v100, v99
	v_cmp_le_i32_e64 s[36:37], s68, v97
	s_and_b64 s[42:43], s[34:35], s[0:1]
	s_and_saveexec_b64 s[40:41], s[42:43]
	s_cbranch_execz .LBB0_97
	v_lshlrev_b32_e32 v99, 1, v97
	v_or_b32_e32 v100, 1, v99
	v_min_i32_e32 v100, s67, v100
	v_cndmask_b32_e64 v99, v100, v99, s[38:39]
	v_add_u32_e32 v100, s66, v99
	v_ashrrev_i32_e32 v101, 31, v100
	v_lshlrev_b64 v[100:101], 8, v[100:101]
	v_lshl_add_u64 v[100:101], v[72:73], 0, v[100:101]
	global_load_dwordx4 v[112:115], v[100:101], off nt
.LBB0_97:
	s_or_b64 exec, exec, s[40:41]
	v_cmp_lt_i32_e32 vcc, v2, v83
	v_add_u32_e32 v2, v2, v85
	v_ashrrev_i32_e32 v54, 31, v2
	s_and_b64 s[30:31], s[34:35], vcc
	v_cndmask_b32_e64 v57, 0, v54, s[30:31]
	v_cndmask_b32_e64 v56, 0, v2, s[30:31]
	v_and_b32_e32 v2, 0x10000, v55
	v_lshlrev_b32_e32 v54, 7, v55
	v_and_b32_e32 v54, 0x7fff80, v54
	v_cmp_eq_u32_e32 vcc, 0, v2
	v_lshl_add_u64 v[56:57], v[56:57], 2, s[58:59]
	global_load_dword v98, v[56:57], off
	v_cndmask_b32_e32 v2, 0, v54, vcc
	v_lshlrev_b32_e32 v2, 1, v2
	v_lshl_add_u64 v[54:55], v[74:75], 0, v[2:3]
	global_load_dwordx4 v[66:69], v[54:55], off
	global_load_dwordx4 v[62:65], v[54:55], off offset:64
	global_load_dwordx4 v[58:61], v[54:55], off offset:128
	s_nop 0
	global_load_dwordx4 v[54:57], v[54:55], off offset:192
	s_waitcnt vmcnt(3)
	v_mfma_f32_16x16x32_f16 v[104:107], v[66:69], v[6:9], 0
	v_or_b32_e32 v2, v108, v79
	v_cmp_lt_i32_e64 s[42:43], v2, v5
	v_cmp_ge_i32_e64 s[40:41], v2, v5
	s_waitcnt vmcnt(2)
	v_mfma_f32_16x16x32_f16 v[104:107], v[62:65], v[10:13], v[104:107]
	s_and_b64 s[42:43], vcc, s[42:43]
	v_cndmask_b32_e64 v2, 0, 1, s[42:43]
	s_and_b64 s[40:41], s[40:41], vcc
	v_cmp_ne_u32_e64 s[42:43], 0, v2
	v_cndmask_b32_e64 v2, 0, 1, s[40:41]
	s_waitcnt vmcnt(1)
	v_mfma_f32_16x16x32_f16 v[104:107], v[58:61], v[14:17], v[104:107]
	v_cmp_ne_u32_e32 vcc, 0, v2
	v_mov_b32_e32 v5, s42
	v_cmp_ngt_f32_e64 s[48:49], s70, v103
	v_mov_b32_e32 v2, vcc_lo
	v_cndmask_b32_e64 v2, v2, v5, s[38:39]
	s_waitcnt vmcnt(0)
	v_mfma_f32_16x16x32_f16 v[108:111], v[54:57], v[18:21], v[104:107]
	v_lshrrev_b32_sdwa v2, v88, v2 dst_sel:DWORD dst_unused:UNUSED_PAD src0_sel:DWORD src1_sel:WORD_0
	v_and_b32_e32 v5, 1, v2
	v_cmp_eq_u32_e64 s[46:47], 0, v5
	v_and_b32_e32 v5, 2, v2
	v_cmp_eq_u32_e64 s[40:41], 0, v5
	v_and_b32_e32 v104, 4, v2
	v_and_b32_e32 v2, 8, v2
	s_nop 0
	v_cndmask_b32_e64 v107, v108, v71, s[46:47]
	v_cndmask_b32_e64 v105, v109, v71, s[40:41]
	v_cmp_eq_u32_e64 s[42:43], 0, v104
	v_cmp_eq_u32_e64 s[44:45], 0, v2
	v_max3_f32 v5, v107, s69, v105
	v_cndmask_b32_e64 v106, v110, v71, s[42:43]
	v_cndmask_b32_e64 v104, v111, v71, s[44:45]
	v_max3_f32 v2, v5, v106, v104
	ds_bpermute_b32 v5, v90, v2
	s_waitcnt lgkmcnt(0)
	v_max_f32_e32 v5, v5, v5
	v_max_f32_e32 v2, v2, v5
	ds_bpermute_b32 v5, v91, v2
	s_waitcnt lgkmcnt(0)
	v_max_f32_e32 v5, v5, v5
	v_max_f32_e32 v108, v2, v5
	v_sub_f32_e32 v2, v108, v103
	v_cmp_lt_f32_e32 vcc, s71, v2
	s_and_b64 vcc, s[48:49], vcc
	s_nop 0
	v_cndmask_b32_e64 v2, 0, 1, vcc
	v_cmp_ne_u32_e64 s[50:51], 0, v2
	s_cmp_lg_u64 s[50:51], 0
	s_cselect_b64 s[50:51], -1, 0
	s_cbranch_vccz .LBB0_117
	v_max_f32_e32 v2, v108, v108
	v_max_f32_e32 v5, v103, v103
	v_max_f32_e32 v5, v5, v2
	v_sub_f32_e32 v2, v103, v5
	v_exp_f32_e32 v2, v2
	s_cbranch_execnz .LBB0_100

.LBB0_102:
	v_sub_f32_e32 v105, v105, v5
	v_sub_f32_e32 v104, v104, v5
	v_exp_f32_e32 v105, v105
	v_exp_f32_e32 v104, v104
	v_sub_f32_e32 v103, v107, v5
	ds_write2_b64 v92, v[66:67], v[68:69] offset1:4
	ds_write2_b64 v92, v[62:63], v[64:65] offset0:8 offset1:12
	ds_read_b64_tr_b16 v[62:63], v93
	ds_read_b64_tr_b16 v[64:65], v93 offset:32
	v_cndmask_b32_e64 v107, v105, 0, s[40:41]
	v_cndmask_b32_e64 v108, v104, 0, s[44:45]
	ds_read_b64_tr_b16 v[68:69], v93 offset:64
	ds_read_b64_tr_b16 v[104:105], v93 offset:96
	ds_write2_b64 v92, v[58:59], v[60:61] offset1:4
	ds_write2_b64 v92, v[54:55], v[56:57] offset0:8 offset1:12
	ds_read_b64_tr_b16 v[54:55], v93
	v_sub_f32_e32 v106, v106, v5
	v_exp_f32_e32 v103, v103
	v_exp_f32_e32 v106, v106
	ds_read_b64_tr_b16 v[56:57], v93 offset:32
	ds_read_b64_tr_b16 v[58:59], v93 offset:64
	ds_read_b64_tr_b16 v[60:61], v93 offset:96
	v_cndmask_b32_e64 v103, v103, 0, s[46:47]
	v_cndmask_b32_e64 v106, v106, 0, s[42:43]
	v_cvt_pk_f16_f32 v67, v106, v108
	v_cvt_pk_f16_f32 v66, v103, v107
	s_waitcnt lgkmcnt(3)
	s_nop 0
	v_mfma_f32_16x16x16_f16 v[30:33], v[54:55], v[66:67], v[30:33]
	v_add_f32_e32 v54, 0, v103
	v_add_f32_e32 v54, v107, v54
	v_add_f32_e32 v54, v106, v54
	v_mfma_f32_16x16x16_f16 v[46:49], v[62:63], v[66:67], v[46:49]
	v_add_f32_e32 v54, v108, v54
	v_fmac_f32_e32 v54, v4, v2
	v_mfma_f32_16x16x16_f16 v[50:53], v[64:65], v[66:67], v[50:53]
	v_mfma_f32_16x16x16_f16 v[38:41], v[68:69], v[66:67], v[38:41]
	v_mfma_f32_16x16x16_f16 v[42:45], v[104:105], v[66:67], v[42:45]
	s_waitcnt lgkmcnt(2)
	v_mfma_f32_16x16x16_f16 v[34:37], v[56:57], v[66:67], v[34:37]
	s_waitcnt lgkmcnt(1)
	v_mfma_f32_16x16x16_f16 v[22:25], v[58:59], v[66:67], v[22:25]
	s_waitcnt lgkmcnt(0)
	v_mfma_f32_16x16x16_f16 v[26:29], v[60:61], v[66:67], v[26:29]
	s_and_saveexec_b64 s[40:41], s[0:1]
	s_cbranch_execz .LBB0_108
	ds_bpermute_b32 v2, v90, v54
	v_mov_b32_e32 v99, v112
	v_mov_b32_e32 v100, v113
	v_mov_b32_e32 v101, v114
	v_mov_b32_e32 v102, v115
	s_waitcnt lgkmcnt(0)
	v_add_f32_e32 v54, v54, v2
	ds_bpermute_b32 v55, v91, v54
	v_lshlrev_b32_e32 v2, 1, v80
	v_or_b32_e32 v4, 1, v2
	v_cmp_gt_i32_e32 vcc, s33, v4
	ds_read_b128 v[4:7], v86 offset:32768
	ds_read_b128 v[8:11], v86 offset:33792
	ds_read_b128 v[12:15], v86 offset:34816
	ds_read_b128 v[16:19], v86 offset:35840
	v_cvt_pk_f16_f32 v53, v52, v53
	v_cvt_pk_f16_f32 v52, v50, v51
	v_cvt_pk_f16_f32 v51, v48, v49
	v_cvt_pk_f16_f32 v50, v46, v47
	v_cvt_pk_f16_f32 v45, v44, v45
	v_cvt_pk_f16_f32 v44, v42, v43
	v_cvt_pk_f16_f32 v43, v40, v41
	v_cvt_pk_f16_f32 v42, v38, v39
	v_cvt_pk_f16_f32 v37, v36, v37
	v_cvt_pk_f16_f32 v36, v34, v35
	v_cvt_pk_f16_f32 v35, v32, v33
	v_cvt_pk_f16_f32 v34, v30, v31
	ds_read_b128 v[30:33], v86 offset:36864
	ds_read_b128 v[38:41], v86 offset:37888
	ds_read_b128 v[46:49], v86 offset:38912
	ds_read_b128 v[56:59], v86 offset:39936
	v_cvt_pk_f16_f32 v63, v28, v29
	v_cvt_pk_f16_f32 v62, v26, v27
	v_cvt_pk_f16_f32 v61, v24, v25
	v_cvt_pk_f16_f32 v60, v22, v23
	s_waitcnt lgkmcnt(7)
	v_mfma_f32_16x16x32_f16 v[4:7], v[4:7], v[50:53], 0
	s_waitcnt lgkmcnt(6)
	v_mfma_f32_16x16x32_f16 v[4:7], v[8:11], v[42:45], v[4:7]
	s_waitcnt lgkmcnt(5)
	v_mfma_f32_16x16x32_f16 v[4:7], v[12:15], v[34:37], v[4:7]
	s_waitcnt lgkmcnt(4)
	v_mfma_f32_16x16x32_f16 v[12:15], v[16:19], v[60:63], v[4:7]
	ds_read_b128 v[8:11], v86 offset:44032
	ds_read_b128 v[16:19], v86 offset:43008
	ds_read_b128 v[20:23], v86 offset:41984
	ds_read_b128 v[24:27], v86 offset:40960
	s_waitcnt lgkmcnt(7)
	v_mfma_f32_16x16x32_f16 v[4:7], v[30:33], v[50:53], 0
	s_waitcnt lgkmcnt(6)
	v_mfma_f32_16x16x32_f16 v[4:7], v[38:41], v[42:45], v[4:7]
	s_waitcnt lgkmcnt(5)
	v_mfma_f32_16x16x32_f16 v[4:7], v[46:49], v[34:37], v[4:7]
	s_waitcnt lgkmcnt(4)
	v_mfma_f32_16x16x32_f16 v[4:7], v[56:59], v[60:63], v[4:7]
	ds_read_b128 v[28:31], v86 offset:45056
	ds_read_b128 v[38:41], v86 offset:46080
	ds_read_b128 v[46:49], v86 offset:47104
	ds_read_b128 v[56:59], v86 offset:48128
	s_waitcnt lgkmcnt(4)
	v_mfma_f32_16x16x32_f16 v[24:27], v[24:27], v[50:53], 0
	v_mfma_f32_16x16x32_f16 v[20:23], v[20:23], v[42:45], v[24:27]
	v_mfma_f32_16x16x32_f16 v[16:19], v[16:19], v[34:37], v[20:23]
	v_mfma_f32_16x16x32_f16 v[8:11], v[8:11], v[60:63], v[16:19]
	s_nop 5
	ds_read_b128 v[20:23], v86 offset:52224
	ds_read_b128 v[24:27], v86 offset:51200
	ds_read_b128 v[64:67], v86 offset:50176
	ds_read_b128 v[104:107], v86 offset:49152
	s_waitcnt lgkmcnt(7)
	v_mfma_f32_16x16x32_f16 v[16:19], v[28:31], v[50:53], 0
	s_waitcnt lgkmcnt(6)
	v_mfma_f32_16x16x32_f16 v[16:19], v[38:41], v[42:45], v[16:19]
	s_waitcnt lgkmcnt(5)
	v_mfma_f32_16x16x32_f16 v[16:19], v[46:49], v[34:37], v[16:19]
	s_waitcnt lgkmcnt(4)
	v_mfma_f32_16x16x32_f16 v[16:19], v[56:59], v[60:63], v[16:19]
	ds_read_b128 v[28:31], v86 offset:53248
	ds_read_b128 v[38:41], v86 offset:54272
	ds_read_b128 v[46:49], v86 offset:55296
	ds_read_b128 v[56:59], v86 offset:56320
	s_waitcnt lgkmcnt(4)
	v_mfma_f32_16x16x32_f16 v[104:107], v[104:107], v[50:53], 0
	v_mfma_f32_16x16x32_f16 v[64:67], v[64:67], v[42:45], v[104:107]
	v_mfma_f32_16x16x32_f16 v[24:27], v[24:27], v[34:37], v[64:67]
	v_mfma_f32_16x16x32_f16 v[20:23], v[20:23], v[60:63], v[24:27]
	s_nop 5
	ds_read_b128 v[64:67], v86 offset:60416
	ds_read_b128 v[104:107], v86 offset:59392
	ds_read_b128 v[108:111], v86 offset:58368
	ds_read_b128 v[112:115], v86 offset:57344
	s_waitcnt lgkmcnt(7)
	v_mfma_f32_16x16x32_f16 v[24:27], v[28:31], v[50:53], 0
	s_waitcnt lgkmcnt(6)
	v_mfma_f32_16x16x32_f16 v[24:27], v[38:41], v[42:45], v[24:27]
	s_waitcnt lgkmcnt(5)
	v_mfma_f32_16x16x32_f16 v[24:27], v[46:49], v[34:37], v[24:27]
	s_waitcnt lgkmcnt(4)
	v_mfma_f32_16x16x32_f16 v[24:27], v[56:59], v[60:63], v[24:27]
	ds_read_b128 v[38:41], v86 offset:61440
	ds_read_b128 v[46:49], v86 offset:62464
	ds_read_b128 v[56:59], v86 offset:63488
	ds_read_b128 v[116:119], v86 offset:64512
	s_waitcnt lgkmcnt(4)
	v_mfma_f32_16x16x32_f16 v[28:31], v[112:115], v[50:53], 0
	v_mfma_f32_16x16x32_f16 v[28:31], v[108:111], v[42:45], v[28:31]
	v_mfma_f32_16x16x32_f16 v[28:31], v[104:107], v[34:37], v[28:31]
	v_mfma_f32_16x16x32_f16 v[28:31], v[64:67], v[60:63], v[28:31]
	s_waitcnt lgkmcnt(3)
	v_mfma_f32_16x16x32_f16 v[38:41], v[38:41], v[50:53], 0
	s_waitcnt lgkmcnt(2)
	v_mfma_f32_16x16x32_f16 v[38:41], v[46:49], v[42:45], v[38:41]
	s_waitcnt lgkmcnt(1)
	v_mfma_f32_16x16x32_f16 v[32:35], v[56:59], v[34:37], v[38:41]
	s_waitcnt lgkmcnt(0)
	v_mfma_f32_16x16x32_f16 v[32:35], v[116:119], v[60:63], v[32:35]
	s_or_b64 s[42:43], s[38:39], vcc
	s_and_saveexec_b64 s[0:1], s[42:43]
	s_cbranch_execz .LBB0_105
	s_nop 0
	global_load_dwordx4 v[36:39], v[76:77], off
	v_cndmask_b32_e64 v12, 0, v12, s[14:15]
	v_cndmask_b32_e64 v13, 0, v13, s[14:15]
	v_cndmask_b32_e64 v14, 0, v14, s[14:15]
	v_cndmask_b32_e64 v15, 0, v15, s[14:15]
	v_cndmask_b32_e64 v7, v15, v7, s[12:13]
	v_cndmask_b32_e64 v6, v14, v6, s[12:13]
	v_cndmask_b32_e64 v5, v13, v5, s[12:13]
	v_cndmask_b32_e64 v4, v12, v4, s[12:13]
	v_add_f32_e32 v40, v54, v55
	v_cndmask_b32_e64 v4, v4, v8, s[10:11]
	v_cndmask_b32_e64 v5, v5, v9, s[10:11]
	v_cndmask_b32_e64 v6, v6, v10, s[10:11]
	v_cndmask_b32_e64 v7, v7, v11, s[10:11]
	v_rcp_f32_e32 v12, v40
	v_cndmask_b32_e64 v7, v7, v19, s[8:9]
	v_cndmask_b32_e64 v6, v6, v18, s[8:9]
	v_cndmask_b32_e64 v5, v5, v17, s[8:9]
	v_cndmask_b32_e64 v4, v4, v16, s[8:9]
	v_cndmask_b32_e64 v4, v4, v20, s[6:7]
	v_cndmask_b32_e64 v5, v5, v21, s[6:7]
	v_cndmask_b32_e64 v6, v6, v22, s[6:7]
	v_cndmask_b32_e64 v7, v7, v23, s[6:7]
	v_cndmask_b32_e64 v7, v7, v27, s[20:21]
	v_cndmask_b32_e64 v6, v6, v26, s[20:21]
	v_cndmask_b32_e64 v5, v5, v25, s[20:21]
	v_cndmask_b32_e64 v4, v4, v24, s[20:21]
	v_cmp_lt_f32_e32 vcc, 0, v40
	v_cndmask_b32_e64 v4, v4, v28, s[18:19]
	v_cndmask_b32_e64 v5, v5, v29, s[18:19]
	v_cndmask_b32_e64 v6, v6, v30, s[18:19]
	v_cndmask_b32_e64 v7, v7, v31, s[18:19]
	v_cndmask_b32_e32 v8, 0, v12, vcc
	v_cndmask_b32_e64 v7, v7, v35, s[16:17]
	v_cndmask_b32_e64 v6, v6, v34, s[16:17]
	v_cndmask_b32_e64 v5, v5, v33, s[16:17]
	v_cndmask_b32_e64 v4, v4, v32, s[16:17]
	v_or_b32_e32 v2, v2, v89
	s_waitcnt vmcnt(0)
	v_fma_mixlo_f16 v4, v8, v4, v36
	v_fma_mixlo_f16 v5, v8, v5, v37
	v_fma_mixlo_f16 v6, v8, v6, v38
	v_fma_mixlo_f16 v7, v8, v7, v39
	v_cndmask_b32_e32 v4, 0, v4, vcc
	v_cndmask_b32_e32 v8, 0, v5, vcc
	v_cndmask_b32_e32 v5, 0, v6, vcc
	v_cndmask_b32_e32 v6, 0, v7, vcc
	v_pack_b32_f16 v5, v5, v6
	v_pack_b32_f16 v4, v4, v8
	v_mad_u64_u32 v[6:7], s[42:43], v2, s72, v[78:79]
	ds_write_b64 v6, v[4:5]
